# baseline (speedup 1.0000x reference)
.LBB0_285:
	v_mul_f32_e32 v250, v147, v241
	v_cmp_class_f32_e64 s[82:83], v240, 64
	v_mul_f32_e32 v251, v151, v243
	v_cmp_class_f32_e64 s[84:85], v242, 64
	v_fma_f32 v24, v250, v54, v24
	v_fma_f32 v25, v251, v54, v25
	v_cndmask_b32_e64 v250, -v148, v173, s[82:83]
	v_cndmask_b32_e64 v251, -v152, v173, s[84:85]
	v_fmac_f32_e32 v24, v250, v55
	v_fmac_f32_e32 v25, v251, v55
	v_med3_f32 v24, v24, v89, 0
	v_med3_f32 v25, v25, v90, 0
	v_mul_f32_e32 v224, v146, v24
	v_mul_f32_e32 v225, v150, v25
	v_add_u16_e32 v208, 0x1000, v208
	v_add_u16_e32 v209, 0x1000, v209
	v_add_u16_e32 v210, 0x1000, v210
	v_add_u16_e32 v211, 0x1000, v211
	v_add_u16_e32 v212, 0x1000, v212
	v_add_u16_e32 v213, 0x1000, v213
	v_add_u16_e32 v214, 0x1000, v214
	v_add_u16_e32 v215, 0x1000, v215
	s_cmp_eq_u64 s[18:19], 0
	s_cbranch_scc1 .Lmy_no89
	v_mul_f32_e32 v250, v123, v245
	v_cmp_class_f32_e64 s[82:83], v244, 64
	v_mul_f32_e32 v251, v124, v247
	v_cmp_class_f32_e64 s[84:85], v246, 64
	v_fma_f32 v26, v250, v54, v26
	v_fma_f32 v27, v251, v54, v27
	v_cndmask_b32_e64 v250, -v125, v173, s[82:83]
	v_cndmask_b32_e64 v251, -v126, v173, s[84:85]
	v_fmac_f32_e32 v26, v250, v55
	v_fmac_f32_e32 v27, v251, v55
	v_med3_f32 v26, v26, v91, 0
	v_med3_f32 v27, v27, v92, 0
	v_mul_f32_e32 v226, v121, v26
	v_mul_f32_e32 v227, v122, v27
	v_add_u16_e32 v216, 0x1000, v216
	v_add_u16_e32 v217, 0x1000, v217

.LBB0_318:
	v_mul_f32_e32 v250, v129, v229
	v_add_f32_dpp v12, v180, v180 row_ror:8 row_mask:0xf bank_mask:0xf bound_ctrl:1
	v_mov_b32_e32 v61, v13
	v_cndmask_b32_e64 v46, v176, 5, s[16:17]
	v_cmp_class_f32_e64 s[82:83], v228, 64
	v_add_f32_dpp v12, v12, v12 row_ror:4 row_mask:0xf bank_mask:0xf bound_ctrl:1
	s_mov_b64 s[60:61], s[16:17]
	v_mul_f32_e32 v251, v132, v231
	v_cmp_class_f32_e64 s[84:85], v230, 64
	v_add_f32_dpp v60, v12, v12 row_ror:2 row_mask:0xf bank_mask:0xf bound_ctrl:1
	v_mov_b32_e32 v12, 48
	v_fma_f32 v18, v250, v54, v18
	v_fma_f32 v19, v251, v54, v19
	v_mov_b32_dpp v61, v60 row_ror:1 row_mask:0xf bank_mask:0xf
	s_and_saveexec_b64 s[58:59], s[10:11]
	s_cbranch_execz .LBB0_286
	v_cndmask_b32_e64 v250, -v130, v173, s[82:83]
	v_add_f32_e32 v12, v60, v61
	v_cvt_f64_f32_e32 v[248:249], v12
	v_cndmask_b32_e64 v251, -v133, v173, s[84:85]
	v_fmac_f32_e32 v18, v250, v55
	v_fmac_f64_e32 v[248:249], v[0:1], v[10:11]
	v_cmp_gt_i32_e32 vcc, 1, v46
	v_mov_b32_e32 v12, 0
	v_fmac_f32_e32 v19, v251, v55
	v_med3_f32 v18, v18, v71, 0
	v_med3_f32 v19, v19, v81, 0
	v_cndmask_b32_e32 v1, 0, v249, vcc
	v_cndmask_b32_e32 v0, 0, v248, vcc
	s_waitcnt lgkmcnt(0)
	v_cvt_f64_f32_e32 v[248:249], v179
	v_mul_f32_e32 v218, v9, v18
	v_mul_f32_e32 v219, v131, v19
	v_add_f64 v[0:1], v[0:1], v[248:249]
	v_mul_f32_e32 v250, v135, v233
	v_cmp_class_f32_e64 s[82:83], v232, 64
	v_mul_f32_e32 v251, v138, v235
	v_cmp_le_f64_e32 vcc, 1.0, v[0:1]
	v_cmp_class_f32_e64 s[84:85], v234, 64
	v_fma_f32 v20, v250, v54, v20
	v_fma_f32 v21, v251, v54, v21
	s_lshr_b32 s11, vcc_lo, 15
	s_and_b32 s10, vcc_lo, 1
	s_and_b32 s11, s11, 2
	s_or_b32 s60, s11, s10
	s_lshr_b64 s[10:11], vcc, 30
	s_and_b32 s10, s10, 4
	s_lshr_b32 s11, vcc_hi, 13
	s_or_b32 s10, s60, s10
	s_and_b32 s11, s11, 8
	s_or_b32 s10, s10, s11
	v_lshlrev_b32_e64 v248, v163, s10
	s_and_saveexec_b64 s[10:11], s[4:5]
	v_and_b32_e32 v12, 3, v178
	v_lshl_or_b32 v12, v12, 2, v175
	v_or_b32_e32 v249, 0x10000, v248
	ds_add_rtn_u32 v12, v12, v249
	s_or_b64 exec, exec, s[10:11]
	v_cndmask_b32_e64 v250, -v136, v173, s[82:83]
	v_cndmask_b32_e64 v251, -v139, v173, s[84:85]
	v_fmac_f32_e32 v20, v250, v55
	v_fmac_f32_e32 v21, v251, v55
	v_med3_f32 v20, v20, v85, 0
	v_med3_f32 v21, v21, v86, 0
	v_mul_f32_e32 v220, v134, v20
	v_mul_f32_e32 v221, v137, v21
	v_mul_f32_e32 v250, v141, v237
	v_cmp_class_f32_e64 s[82:83], v236, 64
	v_mul_f32_e32 v251, v144, v239
	v_cmp_class_f32_e64 s[84:85], v238, 64
	v_fma_f32 v22, v250, v54, v22
	v_fma_f32 v23, v251, v54, v23
	v_cndmask_b32_e64 v250, -v142, v173, s[82:83]
	v_cndmask_b32_e64 v251, -v145, v173, s[84:85]
	v_fmac_f32_e32 v22, v250, v55
	v_fmac_f32_e32 v23, v251, v55
	v_med3_f32 v22, v22, v87, 0
	v_med3_f32 v23, v23, v88, 0
	v_mul_f32_e32 v222, v140, v22
	v_mul_f32_e32 v223, v143, v23
	s_waitcnt lgkmcnt(0)
	v_readfirstlane_b32 s60, v12
	s_and_b32 s10, s60, 0xffff0000
	s_cmp_lg_u32 s10, 0x30000
	s_cbranch_scc1 .LBB0_285
	s_and_saveexec_b64 s[10:11], s[0:1]
	s_cbranch_execz .LBB0_324
	v_lshl_add_u32 v12, v177, 20, s70
	v_add_u32_e32 v248, s60, v248
	v_and_or_b32 v60, v248, s71, v12
	v_lshlrev_b32_e32 v12, 3, v178
	v_and_or_b32 v12, v12, 24, s75
	v_lshl_add_u32 v12, v12, 10, v170
	v_lshl_add_u64 v[248:249], v[12:13], 2, s[14:15]
	global_store_dword v[248:249], v60, off sc0
	v_lshlrev_b64 v[248:249], 7, v[12:13]
	v_lshl_add_u64 v[248:249], s[66:67], 0, v[248:249]
	global_store_dword v[248:249], v60, off sc1
